# static priority raise for waves 4-7 during the attention loop
# speedup vs baseline: 1.0152x; 1.0152x over previous
; #define LAS __attribute__((address_space(3)))
; __device__ __forceinline__ void phase_attn(Frame& F) {
;     ...
;     int jl = r8;
;     if (jl >= PER_X) return;
;     AttnUnit cu = attn_decode(x8 * PER_X + jl);
;     attn_issue(qkv, cu, tid, kr, vr);
;     { const char* qb = (const char*)qkv + (((size_t)cu.b * SEQ + cu.r) * NPROJ + cu.h * 64) * 2; const unsigned qo = __umul24((unsigned)(128 * cu.n + ql), (unsigned)cu.d * (NPROJ * 2)) + 16u * fq;
;       qn0 = *(const bf16x8*)(qb + qo); qn1 = *(const bf16x8*)(qb + qo + 64); }
; #pragma unroll
;     for (int jj = 0; jj < 4; ++jj) { const int ch = tid + 512 * jj, row = ch >> 3, c16 = ch & 7;
;         *(LAS u32x4*)(F.lds + row * ATT_ROWB + c16 * 16) = kr[jj]; *(LAS u32x4*)(F.lds + ATT_VOFF + row * ATT_ROWB + c16 * 16) = vr[jj]; }
;     const int jlast = r8 + G8 * ((PER_X - 1 - r8) / G8);
;     un = attn_decode(x8 * PER_X + (jl + G8 < jlast ? jl + G8 : jlast)); attn_issue(qkv, un, tid, kr, vr);
;     int buf = 0;
;     for (; jl < PER_X; jl += G8) {
;     ...
;         cu = nu; buf ^= 1;
.Lcva_vcu:
	s_lshr_b32 s99, s99, 6
	s_lshl_b32 s101, s101, 3
	s_add_u32 s89, s101, s99
	s_movk_i32 s90, 12
	s_mov_b32 s32, 0
	s_mov_b32 s95, 0
	s_mov_b32 s100, 0
	s_cmp_ge_u32 s99, 4
	s_cbranch_scc0 .Lcq_noprio
	s_setprio 1
.Lcq_noprio:
	s_waitcnt vmcnt(0)
	s_branch .LBB0_304
.LBB0_303:
	s_or_b64 exec, exec, s[64:65]
	s_add_i32 s70, s70, s69
	s_cmpk_lt_i32 s70, 0x600
	s_mov_b32 s35, s74
	s_mov_b32 s34, s36
	s_mov_b32 s30, s75
	s_mov_b32 s26, s72
	s_mov_b32 s31, s73
	s_mov_b32 s64, s76
	s_mov_b32 s36, s58
	s_mov_b32 s75, s80
	s_mov_b32 s74, s82
	s_mov_b32 s72, s81
	s_mov_b32 s73, s83
	s_mov_b32 s76, s84
	s_cbranch_scc0 .LBB0_306

; __device__ __forceinline__ void phase_attn(Frame& F) {
;     ...
;         cu = nu; buf ^= 1;
;     }
;     __syncthreads();
.LBB0_306:
	s_waitcnt vmcnt(0)
	s_setprio 0
